# P0: cvt_rows_i4/cvt_rows_v4 row loops software-pipelined (next row prefetched into spare VGPRs)
# speedup vs baseline: 1.0150x; 1.0038x over previous
.LBB0_49:
	s_or_b64 exec, exec, s[4:5]
	v_readlane_b32 s6, v253, 0
	v_readlane_b32 s7, v253, 1
	v_mov_b32_e32 v2, v175
	v_readlane_b32 s2, v253, 8
	v_ashrrev_i32_e32 v1, 6, v2
	v_and_b32_e32 v8, 64, v24
	v_add_u32_e32 v0, s2, v1
	s_mov_b32 s2, 0x8000
	v_cmp_gt_i32_e32 vcc, s2, v0
	v_xor_b32_e32 v30, 32, v24
	v_xor_b32_e32 v29, 16, v24
	v_xor_b32_e32 v28, 8, v24
	v_xor_b32_e32 v27, 4, v24
	v_xor_b32_e32 v26, 2, v24
	v_xor_b32_e32 v25, 1, v24
	s_and_saveexec_b64 s[4:5], vcc
	s_cbranch_execz .LBB0_54
	v_and_b32_e32 v3, 63, v2
	v_add_u32_e32 v2, 64, v8
	v_xor_b32_e32 v4, 32, v24
	v_cmp_lt_i32_e32 vcc, v4, v2
	s_load_dwordx2 s[8:9], s[6:7], 0xe0
	v_lshlrev_b32_e32 v1, 1, v1
	v_cndmask_b32_e32 v4, v24, v4, vcc
	v_lshlrev_b32_e32 v9, 2, v4
	v_xor_b32_e32 v4, 16, v24
	v_cmp_lt_i32_e32 vcc, v4, v2
	v_readlane_b32 s12, v253, 2
	v_readlane_b32 s14, v253, 4
	v_cndmask_b32_e32 v4, v24, v4, vcc
	v_lshlrev_b32_e32 v10, 2, v4
	v_xor_b32_e32 v4, 8, v24
	v_cmp_lt_i32_e32 vcc, v4, v2
	v_readlane_b32 s13, v253, 3
	v_readlane_b32 s15, v253, 5
	v_cndmask_b32_e32 v4, v24, v4, vcc
	v_lshlrev_b32_e32 v11, 2, v4
	v_xor_b32_e32 v4, 4, v24
	v_cmp_lt_i32_e32 vcc, v4, v2
	s_add_u32 s10, s14, 0x13188004
	s_addc_u32 s11, s15, 0
	v_cndmask_b32_e32 v4, v24, v4, vcc
	v_lshlrev_b32_e32 v12, 2, v4
	v_xor_b32_e32 v4, 2, v24
	v_cmp_lt_i32_e32 vcc, v4, v2
	s_mov_b64 s[12:13], 0x11188000
	s_ashr_i32 s87, s86, 31
	v_cndmask_b32_e32 v4, v24, v4, vcc
	v_lshlrev_b32_e32 v13, 2, v4
	v_xor_b32_e32 v4, 1, v24
	v_cmp_lt_i32_e32 vcc, v4, v2
	v_cmp_eq_u32_e64 s[6:7], 0, v3
	s_lshl_b32 s2, s84, 4
	v_cndmask_b32_e32 v2, v24, v4, vcc
	v_lshlrev_b32_e32 v14, 2, v2
	v_lshl_add_u32 v2, s82, 4, v1
	v_ashrrev_i32_e32 v1, 31, v0
	v_lshlrev_b64 v[4:5], 9, v[0:1]
	v_lshl_or_b32 v4, v3, 3, v4
	v_lshlrev_b64 v[6:7], 12, v[0:1]
	v_lshl_add_u64 v[4:5], s[14:15], 0, v[4:5]
	v_lshl_or_b32 v6, v3, 6, v6
	v_lshl_add_u64 v[4:5], v[4:5], 0, s[12:13]
	s_lshl_b64 s[12:13], s[86:87], 9
	s_waitcnt lgkmcnt(0)
	v_lshl_add_u64 v[6:7], s[8:9], 0, v[6:7]
	s_lshl_b64 s[14:15], s[86:87], 12
	s_mov_b64 s[16:17], 0
	s_mov_b32 s3, 0xf800000
	v_mov_b32_e32 v1, 0x260
	s_mov_b32 s18, 0xc1000000
	v_mov_b32_e32 v15, 0x40e00000
	s_movk_i32 s19, 0x7fff
	global_load_dwordx4 v[100:103], v[6:7], off
	global_load_dwordx4 v[112:115], v[6:7], off offset:48
	global_load_dwordx4 v[104:107], v[6:7], off offset:16
	global_load_dwordx4 v[108:111], v[6:7], off offset:32
	s_branch .LBB0_52

.LBB0_52:
	s_waitcnt vmcnt(0)
	v_mov_b32_e32 v18, v100
	v_mov_b32_e32 v19, v101
	v_mov_b32_e32 v20, v102
	v_mov_b32_e32 v21, v103
	v_mov_b32_e32 v32, v112
	v_mov_b32_e32 v33, v113
	v_mov_b32_e32 v34, v114
	v_mov_b32_e32 v35, v115
	v_mov_b32_e32 v36, v104
	v_mov_b32_e32 v37, v105
	v_mov_b32_e32 v38, v106
	v_mov_b32_e32 v39, v107
	v_mov_b32_e32 v40, v108
	v_mov_b32_e32 v41, v109
	v_mov_b32_e32 v42, v110
	v_mov_b32_e32 v43, v111
	v_add_u32_e32 v116, s86, v0
	v_cmp_ge_i32_e32 vcc, s19, v116
	v_lshl_add_u64 v[118:119], v[6:7], 0, s[14:15]
	s_nop 0
	v_cndmask_b32_e32 v118, v6, v118, vcc
	v_cndmask_b32_e32 v119, v7, v119, vcc
	global_load_dwordx4 v[100:103], v[118:119], off
	global_load_dwordx4 v[112:115], v[118:119], off offset:48
	global_load_dwordx4 v[104:107], v[118:119], off offset:16
	global_load_dwordx4 v[108:111], v[118:119], off offset:32
	v_mul_f32_e32 v3, v19, v19
	v_fmac_f32_e32 v3, v18, v18
	v_fmac_f32_e32 v3, v20, v20
	v_fmac_f32_e32 v3, v21, v21
	v_fmac_f32_e32 v3, v36, v36
	v_fmac_f32_e32 v3, v37, v37
	v_fmac_f32_e32 v3, v38, v38
	v_fmac_f32_e32 v3, v39, v39
	v_fmac_f32_e32 v3, v40, v40
	v_fmac_f32_e32 v3, v41, v41
	v_fmac_f32_e32 v3, v42, v42
	v_pk_mul_f32 v[16:17], v[32:33], v[32:33]
	v_fmac_f32_e32 v3, v43, v43
	v_add_f32_e32 v3, v3, v16
	v_pk_mul_f32 v[22:23], v[34:35], v[34:35]
	v_add_f32_e32 v3, v3, v17
	v_add_f32_e32 v3, v3, v22
	v_add_f32_e32 v3, v3, v23
	ds_bpermute_b32 v16, v9, v3
	s_waitcnt lgkmcnt(0)
	v_add_f32_e32 v3, v3, v16
	ds_bpermute_b32 v16, v10, v3
	s_waitcnt lgkmcnt(0)
	v_add_f32_e32 v3, v3, v16
	ds_bpermute_b32 v16, v11, v3
	s_waitcnt lgkmcnt(0)
	v_add_f32_e32 v3, v3, v16
	ds_bpermute_b32 v16, v12, v3
	s_waitcnt lgkmcnt(0)
	v_add_f32_e32 v3, v3, v16
	ds_bpermute_b32 v16, v13, v3
	s_waitcnt lgkmcnt(0)
	v_add_f32_e32 v3, v3, v16
	ds_bpermute_b32 v16, v14, v3
	s_waitcnt lgkmcnt(0)
	v_add_f32_e32 v3, v3, v16
	v_mul_f32_e32 v3, 0x3a800000, v3
	v_mul_f32_e32 v16, 0x4f800000, v3
	v_cmp_gt_f32_e32 vcc, s3, v3
	s_nop 1
	v_cndmask_b32_e32 v3, v3, v16, vcc
	v_sqrt_f32_e32 v16, v3
	s_nop 0
	v_add_u32_e32 v17, -1, v16
	v_add_u32_e32 v22, 1, v16
	v_fma_f32 v23, -v17, v16, v3
	v_fma_f32 v31, -v22, v16, v3
	v_cmp_ge_f32_e64 s[8:9], 0, v23
	s_nop 1
	v_cndmask_b32_e64 v16, v16, v17, s[8:9]
	v_cmp_lt_f32_e64 s[8:9], 0, v31
	s_nop 1
	v_cndmask_b32_e64 v16, v16, v22, s[8:9]
	v_mul_f32_e32 v17, 0x37800000, v16
	v_cndmask_b32_e32 v16, v16, v17, vcc
	v_cmp_class_f32_e32 vcc, v3, v1
	s_nop 1
	v_cndmask_b32_e32 v3, v16, v3, vcc
	v_mul_f32_e32 v16, 0x3eab9f56, v3
	v_div_scale_f32 v3, s[8:9], v16, v16, 1.0
	v_rcp_f32_e32 v17, v3
	v_div_scale_f32 v22, vcc, 1.0, v16, 1.0
	v_fma_f32 v23, -v3, v17, 1.0
	v_fmac_f32_e32 v17, v23, v17
	v_mul_f32_e32 v23, v22, v17
	v_fma_f32 v31, -v3, v23, v22
	v_fmac_f32_e32 v23, v31, v17
	v_fma_f32 v3, -v3, v23, v22
	v_div_fmas_f32 v3, v3, v17, v23
	v_div_fixup_f32 v3, v3, v16, 1.0
	v_cmp_lt_f32_e32 vcc, 0, v16
	s_nop 1
	v_cndmask_b32_e32 v3, 0, v3, vcc
	v_mul_f32_e32 v17, v18, v3
	v_mul_f32_e32 v18, v19, v3
	v_mul_f32_e32 v19, v20, v3
	v_mul_f32_e32 v20, v21, v3
	v_mul_f32_e32 v21, v36, v3
	v_mul_f32_e32 v22, v37, v3
	v_mul_f32_e32 v23, v38, v3
	v_mul_f32_e32 v31, v39, v3
	v_mul_f32_e32 v36, v40, v3
	v_mul_f32_e32 v37, v41, v3
	v_mul_f32_e32 v38, v42, v3
	v_mul_f32_e32 v39, v43, v3
	v_mul_f32_e32 v32, v32, v3
	v_mul_f32_e32 v33, v33, v3
	v_mul_f32_e32 v34, v34, v3
	v_mul_f32_e32 v3, v35, v3
	v_floor_f32_e32 v17, v17
	v_floor_f32_e32 v18, v18
	v_floor_f32_e32 v31, v31
	v_floor_f32_e32 v35, v36
	v_floor_f32_e32 v36, v37
	v_floor_f32_e32 v3, v3
	v_floor_f32_e32 v19, v19
	v_floor_f32_e32 v37, v38
	v_med3_f32 v17, v17, s18, v15
	v_med3_f32 v18, v18, s18, v15
	v_med3_f32 v31, v31, s18, v15
	v_med3_f32 v35, v35, s18, v15
	v_med3_f32 v36, v36, s18, v15
	v_med3_f32 v3, v3, s18, v15
	v_floor_f32_e32 v20, v20
	v_floor_f32_e32 v38, v39
	v_med3_f32 v19, v19, s18, v15
	v_med3_f32 v37, v37, s18, v15
	v_cvt_i32_f32_e32 v35, v35
	v_cvt_i32_f32_e32 v17, v17
	v_cvt_i32_f32_e32 v18, v18
	v_cvt_i32_f32_e32 v36, v36
	v_cvt_i32_f32_e32 v31, v31
	v_cvt_i32_f32_e32 v3, v3
	v_med3_f32 v20, v20, s18, v15
	v_med3_f32 v38, v38, s18, v15
	v_cvt_i32_f32_e32 v19, v19
	v_cvt_i32_f32_e32 v37, v37
	v_floor_f32_e32 v21, v21
	v_floor_f32_e32 v22, v22
	v_floor_f32_e32 v32, v32
	v_floor_f32_e32 v33, v33
	v_cvt_i32_f32_e32 v20, v20
	v_cvt_i32_f32_e32 v38, v38
	v_med3_f32 v21, v21, s18, v15
	v_med3_f32 v22, v22, s18, v15
	v_med3_f32 v32, v32, s18, v15
	v_med3_f32 v33, v33, s18, v15
	v_floor_f32_e32 v23, v23
	v_floor_f32_e32 v34, v34
	v_cvt_i32_f32_sdwa v21, v21 dst_sel:WORD_1 dst_unused:UNUSED_PAD src0_sel:DWORD
	v_cvt_i32_f32_sdwa v32, v32 dst_sel:WORD_1 dst_unused:UNUSED_PAD src0_sel:DWORD
	v_cvt_i32_f32_e32 v22, v22
	v_cvt_i32_f32_e32 v33, v33
	v_and_b32_e32 v35, 15, v35
	v_and_b32_e32 v17, 15, v17
	v_lshlrev_b32_e32 v36, 4, v36
	v_lshlrev_b32_e32 v18, 4, v18
	v_lshlrev_b32_e32 v3, 28, v3
	v_lshlrev_b32_e32 v31, 28, v31
	v_med3_f32 v23, v23, s18, v15
	v_med3_f32 v34, v34, s18, v15
	v_lshlrev_b32_e32 v37, 8, v37
	v_lshlrev_b32_e32 v19, 8, v19
	v_and_b32_e32 v36, 0xf0, v36
	v_and_b32_e32 v18, 0xf0, v18
	v_or_b32_e32 v3, v3, v35
	v_or_b32_e32 v17, v31, v17
	v_cvt_i32_f32_sdwa v23, v23 dst_sel:BYTE_3 dst_unused:UNUSED_PAD src0_sel:DWORD
	v_cvt_i32_f32_sdwa v34, v34 dst_sel:BYTE_3 dst_unused:UNUSED_PAD src0_sel:DWORD
	v_lshlrev_b32_e32 v38, 12, v38
	v_lshlrev_b32_e32 v20, 12, v20
	v_and_b32_e32 v37, 0xf00, v37
	v_and_b32_e32 v19, 0xf00, v19
	v_or_b32_e32 v3, v3, v36
	v_or_b32_e32 v17, v17, v18
	v_and_b32_e32 v38, 0xf000, v38
	v_and_b32_e32 v20, 0xf000, v20
	v_or_b32_e32 v3, v3, v37
	v_or_b32_e32 v17, v17, v19
	v_and_b32_e32 v32, 0xf0000, v32
	v_and_b32_e32 v21, 0xf0000, v21
	v_lshlrev_b32_e32 v33, 20, v33
	v_lshlrev_b32_e32 v22, 20, v22
	v_or_b32_e32 v3, v3, v38
	v_or_b32_e32 v17, v17, v20
	v_and_b32_e32 v33, 0xf00000, v33
	v_and_b32_e32 v22, 0xf00000, v22
	v_or_b32_e32 v3, v3, v32
	v_or_b32_e32 v17, v17, v21
	v_and_b32_e32 v34, 0xf000000, v34
	v_and_b32_e32 v23, 0xf000000, v23
	v_or_b32_e32 v3, v3, v33
	v_or_b32_e32 v17, v17, v22
	v_or_b32_e32 v19, v3, v34
	v_or_b32_e32 v18, v17, v23
	global_store_dwordx2 v[4:5], v[18:19], off
	s_and_saveexec_b64 s[8:9], s[6:7]
	s_cbranch_execz .LBB0_51
	v_ashrrev_i32_e32 v3, 31, v2
	v_lshl_add_u64 v[18:19], v[2:3], 2, s[10:11]
	global_store_dword v[18:19], v16, off
	s_branch .LBB0_51
.LBB0_54:
	s_or_b64 exec, exec, s[4:5]
	v_readlane_b32 s4, v253, 2
	v_readlane_b32 s6, v253, 4
	v_readlane_b32 s7, v253, 5
	s_add_u32 s88, s6, 0x13188000
	s_addc_u32 s89, s7, 0
	v_readlane_b32 s6, v253, 0
	v_readlane_b32 s7, v253, 1
	v_mov_b32_e32 v1, v175
	v_readlane_b32 s2, v253, 8
	v_ashrrev_i32_e32 v0, 6, v1
	v_readlane_b32 s5, v253, 3
	v_add_u32_e32 v16, s2, v0
	s_movk_i32 s2, 0x7fff
	v_cmp_lt_i32_e32 vcc, s2, v16
	s_and_saveexec_b64 s[2:3], vcc
	s_xor_b64 s[4:5], exec, s[2:3]
	v_add_u32_e32 v31, 64, v8
	v_xor_b32_e32 v30, 32, v24
	v_xor_b32_e32 v29, 16, v24
	v_xor_b32_e32 v28, 8, v24
	v_xor_b32_e32 v27, 4, v24
	v_xor_b32_e32 v26, 2, v24
	v_xor_b32_e32 v25, 1, v24
	s_andn2_saveexec_b64 s[4:5], s[4:5]
	s_cbranch_execz .LBB0_62
	v_add_u32_e32 v31, 64, v8
	v_cmp_lt_i32_e32 vcc, v30, v31
	v_and_b32_e32 v2, 63, v1
	v_lshlrev_b32_e32 v0, 1, v0
	v_cndmask_b32_e32 v1, v24, v30, vcc
	v_cmp_lt_i32_e32 vcc, v29, v31
	v_lshlrev_b32_e32 v32, 2, v1
	v_ashrrev_i32_e32 v17, 31, v16
	v_cndmask_b32_e32 v1, v24, v29, vcc
	v_cmp_lt_i32_e32 vcc, v28, v31
	v_lshlrev_b32_e32 v33, 2, v1
	s_load_dwordx2 s[8:9], s[6:7], 0xe8
	v_cndmask_b32_e32 v1, v24, v28, vcc
	v_cmp_lt_i32_e32 vcc, v27, v31
	v_lshlrev_b32_e32 v34, 2, v1
	v_lshl_add_u32 v18, s82, 4, v0
	v_cndmask_b32_e32 v1, v24, v27, vcc
	v_cmp_lt_i32_e32 vcc, v26, v31
	v_lshlrev_b32_e32 v35, 2, v1
	v_readlane_b32 s12, v253, 2
	v_cndmask_b32_e32 v1, v24, v26, vcc
	v_cmp_lt_i32_e32 vcc, v25, v31
	v_lshlrev_b32_e32 v36, 2, v1
	v_readlane_b32 s14, v253, 4
	v_cndmask_b32_e32 v1, v24, v25, vcc
	v_lshlrev_b32_e32 v37, 2, v1
	v_lshlrev_b64 v[0:1], 9, v[16:17]
	v_lshl_or_b32 v0, v2, 3, v0
	v_readlane_b32 s15, v253, 5
	s_mov_b64 s[10:11], 0x12188000
	v_readlane_b32 s13, v253, 3
	v_lshl_add_u64 v[0:1], s[14:15], 0, v[0:1]
	v_lshl_add_u64 v[20:21], v[0:1], 0, s[10:11]
	v_lshlrev_b64 v[0:1], 12, v[16:17]
	s_ashr_i32 s87, s86, 31
	v_lshl_or_b32 v0, v2, 6, v0
	v_cmp_eq_u32_e64 s[6:7], 0, v2
	s_lshl_b32 s2, s84, 4
	s_lshl_b64 s[10:11], s[86:87], 9
	s_waitcnt lgkmcnt(0)
	v_lshl_add_u64 v[22:23], s[8:9], 0, v[0:1]
	s_lshl_b64 s[14:15], s[86:87], 12
	s_mov_b64 s[12:13], 0
	s_mov_b32 s3, 0xf800000
	v_mov_b32_e32 v17, 0x260
	s_mov_b32 s16, 0x3e800000
	s_mov_b32 s17, 0x3f400000
	s_mov_b32 s18, 0x3fb00000
	s_mov_b32 s19, 0x3f880000
	s_mov_b32 s20, 0x3fe00000
	s_mov_b32 s21, 0x40100000
	s_movk_i32 s22, 0x7fff
	global_load_dwordx4 v[100:103], v[22:23], off
	global_load_dwordx4 v[104:107], v[22:23], off offset:16
	global_load_dwordx4 v[108:111], v[22:23], off offset:32
	global_load_dwordx4 v[112:115], v[22:23], off offset:48
	s_branch .LBB0_59

.LBB0_59:
	s_waitcnt vmcnt(0)
	v_mov_b32_e32 v8, v100
	v_mov_b32_e32 v9, v101
	v_mov_b32_e32 v10, v102
	v_mov_b32_e32 v11, v103
	v_mov_b32_e32 v4, v104
	v_mov_b32_e32 v5, v105
	v_mov_b32_e32 v6, v106
	v_mov_b32_e32 v7, v107
	v_mov_b32_e32 v12, v108
	v_mov_b32_e32 v13, v109
	v_mov_b32_e32 v14, v110
	v_mov_b32_e32 v15, v111
	v_mov_b32_e32 v0, v112
	v_mov_b32_e32 v1, v113
	v_mov_b32_e32 v2, v114
	v_mov_b32_e32 v3, v115
	v_add_u32_e32 v116, s86, v16
	v_cmp_ge_i32_e32 vcc, s22, v116
	v_lshl_add_u64 v[118:119], v[22:23], 0, s[14:15]
	s_nop 0
	v_cndmask_b32_e32 v118, v22, v118, vcc
	v_cndmask_b32_e32 v119, v23, v119, vcc
	global_load_dwordx4 v[100:103], v[118:119], off
	global_load_dwordx4 v[104:107], v[118:119], off offset:16
	global_load_dwordx4 v[108:111], v[118:119], off offset:32
	global_load_dwordx4 v[112:115], v[118:119], off offset:48
	v_mul_f32_e32 v19, v9, v9
	v_mov_b32_e32 v38, v11
	v_mov_b32_e32 v39, v4
	v_fmac_f32_e32 v19, v8, v8
	v_pk_mul_f32 v[38:39], v[38:39], v[38:39]
	v_fmac_f32_e32 v19, v10, v10
	v_mov_b32_e32 v40, v5
	v_mov_b32_e32 v41, v6
	v_add_f32_e32 v19, v19, v38
	v_pk_mul_f32 v[40:41], v[40:41], v[40:41]
	v_add_f32_e32 v19, v19, v39
	v_add_f32_e32 v19, v19, v40
	v_add_f32_e32 v19, v19, v41
	v_fmac_f32_e32 v19, v7, v7
	v_fmac_f32_e32 v19, v12, v12
	v_mov_b32_e32 v42, v15
	v_mov_b32_e32 v43, v0
	v_mov_b32_e32 v44, v1
	v_mov_b32_e32 v45, v2
	v_fmac_f32_e32 v19, v13, v13
	v_pk_mov_b32 v[42:43], v[42:43], v[44:45] op_sel:[1,0]
	v_fmac_f32_e32 v19, v14, v14
	v_pk_mul_f32 v[42:43], v[42:43], v[42:43]
	v_fmac_f32_e32 v19, v15, v15
	v_add_f32_e32 v19, v19, v42
	v_pk_mul_f32 v[46:47], v[2:3], v[2:3]
	v_add_f32_e32 v19, v19, v43
	v_add_f32_e32 v19, v19, v46
	v_add_f32_e32 v19, v19, v47
	ds_bpermute_b32 v38, v32, v19
	v_mov_b32_e32 v39, v15
	v_mov_b32_e32 v41, v0
	v_mov_b32_e32 v0, v5
	v_mov_b32_e32 v43, v2
	s_waitcnt lgkmcnt(0)
	v_add_f32_e32 v19, v19, v38
	ds_bpermute_b32 v38, v33, v19
	v_mov_b32_e32 v42, v6
	v_mov_b32_e32 v44, v8
	v_mov_b32_e32 v45, v12
	v_mov_b32_e32 v12, v9
	s_waitcnt lgkmcnt(0)
	v_add_f32_e32 v19, v19, v38
	ds_bpermute_b32 v38, v34, v19
	s_waitcnt lgkmcnt(0)
	v_add_f32_e32 v19, v19, v38
	ds_bpermute_b32 v38, v35, v19
	s_waitcnt lgkmcnt(0)
	v_add_f32_e32 v19, v19, v38
	ds_bpermute_b32 v40, v36, v19
	v_mov_b32_e32 v38, v11
	s_waitcnt lgkmcnt(0)
	v_add_f32_e32 v11, v19, v40
	ds_bpermute_b32 v15, v37, v11
	v_mov_b32_e32 v40, v4
	s_waitcnt lgkmcnt(0)
	v_add_f32_e32 v4, v11, v15
	v_mul_f32_e32 v4, 0x3a800000, v4
	v_mul_f32_e32 v5, 0x4f800000, v4
	v_cmp_gt_f32_e32 vcc, s3, v4
	s_nop 1
	v_cndmask_b32_e32 v4, v4, v5, vcc
	v_sqrt_f32_e32 v5, v4
	s_nop 0
	v_add_u32_e32 v2, -1, v5
	v_add_u32_e32 v6, 1, v5
	v_fma_f32 v8, -v2, v5, v4
	v_fma_f32 v11, -v6, v5, v4
	v_cmp_ge_f32_e64 s[8:9], 0, v8
	s_nop 1
	v_cndmask_b32_e64 v2, v5, v2, s[8:9]
	v_cmp_lt_f32_e64 s[8:9], 0, v11
	s_nop 1
	v_cndmask_b32_e64 v2, v2, v6, s[8:9]
	v_mul_f32_e32 v5, 0x37800000, v2
	v_cndmask_b32_e32 v2, v2, v5, vcc
	v_cmp_class_f32_e32 vcc, v4, v17
	s_nop 1
	v_cndmask_b32_e32 v2, v2, v4, vcc
	v_mul_f32_e32 v5, 0x3f89999a, v2
	v_div_scale_f32 v2, s[8:9], v5, v5, 1.0
	v_rcp_f32_e32 v4, v2
	v_div_scale_f32 v6, vcc, 1.0, v5, 1.0
	v_fma_f32 v8, -v2, v4, 1.0
	v_fmac_f32_e32 v4, v8, v4
	v_mul_f32_e32 v8, v6, v4
	v_fma_f32 v9, -v2, v8, v6
	v_fmac_f32_e32 v8, v9, v4
	v_fma_f32 v2, -v2, v8, v6
	v_div_fmas_f32 v2, v2, v4, v8
	v_div_fixup_f32 v2, v2, v5, 1.0
	v_cmp_lt_f32_e32 vcc, 0, v5
	s_nop 1
	v_cndmask_b32_e32 v4, 0, v2, vcc
	v_pk_mul_f32 v[8:9], v[38:39], v[4:5] op_sel_hi:[1,0]
	v_pk_mul_f32 v[38:39], v[40:41], v[4:5] op_sel_hi:[1,0]
	v_cmp_gt_f32_e64 s[8:9], |v8|, s16
	v_pk_mul_f32 v[40:41], v[0:1], v[4:5] op_sel_hi:[1,0]
	v_pk_mul_f32 v[0:1], v[42:43], v[4:5] op_sel_hi:[1,0]
	v_cndmask_b32_e64 v2, 0, 1, s[8:9]
	v_cmp_gt_f32_e64 s[8:9], |v8|, 0.5
	v_pk_mul_f32 v[42:43], v[44:45], v[4:5] op_sel_hi:[1,0]
	v_cmp_gt_f32_e64 vcc, |v8|, s17
	v_cndmask_b32_e64 v6, 0, 1, s[8:9]
	v_cmp_gt_f32_e64 s[8:9], |v38|, s16
	v_addc_co_u32_e32 v2, vcc, v2, v6, vcc
	s_nop 0
	v_cndmask_b32_e64 v15, 0, 1, s[8:9]
	v_cmp_gt_f32_e64 s[8:9], |v38|, 0.5
	v_pk_mul_f32 v[12:13], v[12:13], v[4:5] op_sel_hi:[1,0]
	v_cmp_gt_f32_e64 vcc, |v42|, s17
	v_cndmask_b32_e64 v19, 0, 1, s[8:9]
	v_cmp_gt_f32_e64 s[8:9], |v42|, s16
	v_lshrrev_b32_e32 v51, 28, v43
	v_lshrrev_b32_e32 v52, 28, v42
	v_cndmask_b32_e64 v11, 0, 1, s[8:9]
	v_cmp_gt_f32_e64 s[8:9], |v42|, 0.5
	s_nop 1
	v_cndmask_b32_e64 v44, 0, 1, s[8:9]
	v_cmp_gt_f32_e64 s[8:9], |v42|, s19
	v_addc_co_u32_e32 v6, vcc, v11, v44, vcc
	s_nop 0
	v_cndmask_b32_e64 v45, 0, 1, s[8:9]
	v_cmp_gt_f32_e64 s[8:9], |v43|, s16
	v_cmp_gt_f32_e64 vcc, |v43|, s17
	v_and_b32_e32 v44, 8, v51
	v_cndmask_b32_e64 v46, 0, 1, s[8:9]
	v_cmp_gt_f32_e64 s[8:9], |v43|, 0.5
	s_nop 1
	v_cndmask_b32_e64 v47, 0, 1, s[8:9]
	v_cmp_gt_f32_e64 s[8:9], |v43|, s19
	v_addc_co_u32_e32 v11, vcc, v46, v47, vcc
	s_nop 0
	v_cndmask_b32_e64 v48, 0, 1, s[8:9]
	v_cmp_gt_f32_e64 s[8:9], |v42|, s20
	v_cmp_gt_f32_e64 vcc, |v12|, s17
	v_and_b32_e32 v46, 8, v52
	v_cndmask_b32_e64 v49, 0, 1, s[8:9]
	v_cmp_gt_f32_e64 s[8:9], |v43|, s20
	s_nop 1
	v_cndmask_b32_e64 v50, 0, 1, s[8:9]
	v_cmp_gt_f32_e64 s[8:9], |v12|, s16
	s_nop 1
	v_cndmask_b32_e64 v53, 0, 1, s[8:9]
	v_cmp_gt_f32_e64 s[8:9], |v12|, 0.5
	s_nop 1
	v_cndmask_b32_e64 v54, 0, 1, s[8:9]
	v_cmp_gt_f32_e64 s[8:9], |v12|, s19
	v_addc_co_u32_e32 v47, vcc, v53, v54, vcc
	s_nop 0
	v_cndmask_b32_e64 v55, 0, 1, s[8:9]
	v_cmp_gt_f32_e64 s[8:9], |v13|, s16
	v_cmp_gt_f32_e64 vcc, |v13|, s17
	s_nop 0
	v_cndmask_b32_e64 v56, 0, 1, s[8:9]
	v_cmp_gt_f32_e64 s[8:9], |v13|, 0.5
	s_nop 1
	v_cndmask_b32_e64 v57, 0, 1, s[8:9]
	v_addc_co_u32_e32 v51, vcc, v56, v57, vcc
	v_cmp_gt_f32_e64 vcc, |v42|, s18
	v_cmp_gt_f32_e64 s[8:9], |v13|, s19
	s_nop 0
	v_addc_co_u32_e32 v6, vcc, v6, v45, vcc
	v_cmp_gt_f32_e64 vcc, |v43|, s18
	v_cndmask_b32_e64 v58, 0, 1, s[8:9]
	v_cmp_gt_f32_e64 s[8:9], |v12|, s20
	v_addc_co_u32_e32 v11, vcc, v11, v48, vcc
	v_cmp_gt_f32_e64 vcc, |v12|, s18
	s_nop 1
	v_addc_co_u32_e32 v45, vcc, v47, v55, vcc
	v_cmp_gt_f32_e64 vcc, |v43|, s21
	v_cndmask_b32_e64 v43, 0, 1, s[8:9]
	v_cmp_gt_f32_e64 s[8:9], |v13|, s20
	v_addc_co_u32_e32 v11, vcc, v11, v50, vcc
	v_cmp_gt_f32_e64 vcc, |v42|, s21
	v_or_b32_e32 v11, v11, v44
	v_cndmask_b32_e64 v44, 0, 1, s[8:9]
	v_addc_co_u32_e32 v6, vcc, v6, v49, vcc
	v_cmp_gt_f32_e64 vcc, |v13|, s18
	v_or_b32_e32 v6, v6, v46
	s_nop 0
	v_addc_co_u32_e32 v42, vcc, v51, v58, vcc
	v_cmp_gt_f32_e64 vcc, |v13|, s21
	v_lshrrev_b32_e32 v13, 28, v13
	v_and_b32_e32 v13, 8, v13
	v_addc_co_u32_e32 v42, vcc, v42, v44, vcc
	v_or_b32_e32 v13, v42, v13
	v_cmp_gt_f32_e64 vcc, |v12|, s21
	v_lshrrev_b32_e32 v12, 28, v12
	v_lshlrev_b32_e32 v13, 4, v13
	v_addc_co_u32_e32 v43, vcc, v45, v43, vcc
	v_and_b32_e32 v12, 8, v12
	v_or_b32_e32 v13, v11, v13
	v_mov_b32_e32 v11, v14
	v_or_b32_e32 v12, v43, v12
	v_pk_mul_f32 v[10:11], v[10:11], v[4:5] op_sel_hi:[1,0]
	v_lshlrev_b32_e32 v12, 4, v12
	v_cmp_gt_f32_e64 s[8:9], |v10|, s16
	v_or_b32_e32 v6, v6, v12
	v_cmp_gt_f32_e64 vcc, |v10|, s17
	v_cndmask_b32_e64 v12, 0, 1, s[8:9]
	v_cmp_gt_f32_e64 s[8:9], |v10|, 0.5
	s_nop 1
	v_cndmask_b32_e64 v14, 0, 1, s[8:9]
	v_cmp_gt_f32_e64 s[8:9], |v10|, s19
	v_addc_co_u32_e32 v12, vcc, v12, v14, vcc
	s_nop 0
	v_cndmask_b32_e64 v14, 0, 1, s[8:9]
	v_cmp_gt_f32_e64 s[8:9], |v11|, s16
	v_cmp_gt_f32_e64 vcc, |v11|, s17
	s_nop 0
	v_cndmask_b32_e64 v42, 0, 1, s[8:9]
	v_cmp_gt_f32_e64 s[8:9], |v11|, 0.5
	s_nop 1
	v_cndmask_b32_e64 v43, 0, 1, s[8:9]
	v_addc_co_u32_e32 v42, vcc, v42, v43, vcc
	v_cmp_gt_f32_e64 vcc, |v10|, s18
	v_cmp_gt_f32_e64 s[8:9], |v11|, s19
	s_nop 0
	v_addc_co_u32_e32 v12, vcc, v12, v14, vcc
	v_cndmask_b32_e64 v43, 0, 1, s[8:9]
	v_cmp_gt_f32_e64 vcc, |v11|, s18
	v_cmp_gt_f32_e64 s[8:9], |v10|, s20
	s_nop 0
	v_addc_co_u32_e32 v14, vcc, v42, v43, vcc
	v_cndmask_b32_e64 v42, 0, 1, s[8:9]
	v_cmp_gt_f32_e64 s[8:9], |v11|, s20
	v_cmp_gt_f32_e64 vcc, |v11|, s21
	v_lshrrev_b32_e32 v11, 28, v11
	v_cndmask_b32_e64 v43, 0, 1, s[8:9]
	v_addc_co_u32_e32 v14, vcc, v14, v43, vcc
	v_cmp_gt_f32_e64 vcc, |v10|, s21
	v_lshrrev_b32_e32 v10, 28, v10
	v_and_b32_e32 v10, 8, v10
	v_addc_co_u32_e32 v12, vcc, v12, v42, vcc
	v_or_b32_e32 v10, v12, v10
	v_lshlrev_b32_e32 v10, 8, v10
	v_cmp_gt_f32_e64 s[8:9], |v9|, s16
	v_and_b32_e32 v11, 8, v11
	v_or_b32_e32 v6, v6, v10
	v_cndmask_b32_e64 v10, 0, 1, s[8:9]
	v_cmp_gt_f32_e64 s[8:9], |v9|, 0.5
	v_or_b32_e32 v11, v14, v11
	v_cmp_gt_f32_e64 vcc, |v9|, s17
	v_cndmask_b32_e64 v12, 0, 1, s[8:9]
	v_cmp_gt_f32_e64 s[8:9], |v9|, s19
	v_lshlrev_b32_e32 v11, 8, v11
	v_addc_co_u32_e32 v10, vcc, v10, v12, vcc
	v_cndmask_b32_e64 v12, 0, 1, s[8:9]
	v_cmp_gt_f32_e64 s[8:9], |v8|, s19
	v_or_b32_e32 v11, v13, v11
	v_cmp_gt_f32_e64 vcc, |v8|, s18
	v_cndmask_b32_e64 v13, 0, 1, s[8:9]
	v_cmp_gt_f32_e64 s[8:9], |v8|, s20
	v_addc_co_u32_e32 v2, vcc, v2, v13, vcc
	v_cmp_gt_f32_e64 vcc, |v9|, s18
	s_nop 1
	v_addc_co_u32_e32 v10, vcc, v10, v12, vcc
	v_cndmask_b32_e64 v12, 0, 1, s[8:9]
	v_cmp_gt_f32_e64 s[8:9], |v9|, s20
	v_cmp_gt_f32_e64 vcc, |v9|, s21
	v_lshrrev_b32_e32 v9, 28, v9
	v_cndmask_b32_e64 v13, 0, 1, s[8:9]
	v_addc_co_u32_e32 v10, vcc, v10, v13, vcc
	v_cmp_gt_f32_e64 vcc, |v8|, s21
	v_lshrrev_b32_e32 v8, 28, v8
	v_and_b32_e32 v8, 8, v8
	v_addc_co_u32_e32 v2, vcc, v2, v12, vcc
	v_or_b32_e32 v2, v2, v8
	v_and_b32_e32 v9, 8, v9
	v_lshlrev_b32_e32 v2, 12, v2
	v_cmp_gt_f32_e64 s[8:9], |v39|, s16
	v_or_b32_e32 v9, v10, v9
	v_or_b32_e32 v2, v6, v2
	v_cndmask_b32_e64 v6, 0, 1, s[8:9]
	v_cmp_gt_f32_e64 s[8:9], |v39|, 0.5
	v_lshlrev_b32_e32 v8, 12, v9
	v_cmp_gt_f32_e64 vcc, |v39|, s17
	v_cndmask_b32_e64 v9, 0, 1, s[8:9]
	v_cmp_gt_f32_e64 s[8:9], |v39|, s19
	v_addc_co_u32_e32 v6, vcc, v6, v9, vcc
	v_cmp_gt_f32_e64 vcc, |v38|, s17
	v_cndmask_b32_e64 v10, 0, 1, s[8:9]
	v_cmp_gt_f32_e64 s[8:9], |v38|, s19
	v_addc_co_u32_e32 v9, vcc, v15, v19, vcc
	v_or_b32_e32 v8, v11, v8
	v_cndmask_b32_e64 v11, 0, 1, s[8:9]
	v_cmp_gt_f32_e64 vcc, |v38|, s18
	v_cmp_gt_f32_e64 s[8:9], |v38|, s20
	s_nop 0
	v_addc_co_u32_e32 v9, vcc, v9, v11, vcc
	v_cmp_gt_f32_e64 vcc, |v39|, s18
	s_nop 1
	v_addc_co_u32_e32 v6, vcc, v6, v10, vcc
	v_cndmask_b32_e64 v10, 0, 1, s[8:9]
	v_cmp_gt_f32_e64 s[8:9], |v39|, s20
	v_cmp_gt_f32_e64 vcc, |v39|, s21
	s_nop 0
	v_cndmask_b32_e64 v11, 0, 1, s[8:9]
	v_addc_co_u32_e32 v6, vcc, v6, v11, vcc
	v_cmp_gt_f32_e64 vcc, |v38|, s21
	v_lshrrev_b32_e32 v11, 28, v38
	v_and_b32_e32 v11, 8, v11
	v_addc_co_u32_e32 v9, vcc, v9, v10, vcc
	v_lshrrev_b32_e32 v10, 28, v39
	v_and_b32_e32 v10, 8, v10
	v_or_b32_sdwa v6, v6, v10 dst_sel:WORD_1 dst_unused:UNUSED_PAD src0_sel:DWORD src1_sel:DWORD
	v_cmp_gt_f32_e64 s[8:9], |v40|, s16
	v_or_b32_sdwa v9, v9, v11 dst_sel:WORD_1 dst_unused:UNUSED_PAD src0_sel:DWORD src1_sel:DWORD
	v_or_b32_e32 v6, v8, v6
	v_cndmask_b32_e64 v8, 0, 1, s[8:9]
	v_cmp_gt_f32_e64 s[8:9], |v41|, s16
	v_or_b32_e32 v2, v2, v9
	v_cmp_gt_f32_e64 vcc, |v41|, s17
	v_cndmask_b32_e64 v9, 0, 1, s[8:9]
	v_cmp_gt_f32_e64 s[8:9], |v40|, 0.5
	s_nop 1
	v_cndmask_b32_e64 v10, 0, 1, s[8:9]
	v_cmp_gt_f32_e64 s[8:9], |v41|, 0.5
	s_nop 1
	v_cndmask_b32_e64 v11, 0, 1, s[8:9]
	v_addc_co_u32_e32 v9, vcc, v9, v11, vcc
	v_cmp_gt_f32_e64 vcc, |v40|, s17
	v_cmp_gt_f32_e64 s[8:9], |v41|, s19
	s_nop 0
	v_addc_co_u32_e32 v8, vcc, v8, v10, vcc
	v_cndmask_b32_e64 v10, 0, 1, s[8:9]
	v_cmp_gt_f32_e64 s[8:9], |v40|, s19
	v_cmp_gt_f32_e64 vcc, |v40|, s18
	s_nop 0
	v_cndmask_b32_e64 v11, 0, 1, s[8:9]
	v_addc_co_u32_e32 v8, vcc, v8, v11, vcc
	v_cmp_gt_f32_e64 vcc, |v41|, s18
	v_cmp_gt_f32_e64 s[8:9], |v40|, s20
	s_nop 0
	v_addc_co_u32_e32 v9, vcc, v9, v10, vcc
	v_cndmask_b32_e64 v10, 0, 1, s[8:9]
	v_cmp_gt_f32_e64 s[8:9], |v41|, s20
	v_cmp_gt_f32_e64 vcc, |v41|, s21
	s_nop 0
	v_cndmask_b32_e64 v11, 0, 1, s[8:9]
	v_addc_co_u32_e32 v9, vcc, v9, v11, vcc
	v_cmp_gt_f32_e64 vcc, |v40|, s21
	v_lshrrev_b32_e32 v11, 28, v40
	v_and_b32_e32 v11, 8, v11
	v_addc_co_u32_e32 v8, vcc, v8, v10, vcc
	v_lshrrev_b32_e32 v10, 28, v41
	v_and_b32_e32 v10, 8, v10
	v_or_b32_e32 v8, v8, v11
	v_or_b32_e32 v9, v9, v10
	v_lshlrev_b32_e32 v8, 20, v8
	v_cmp_gt_f32_e64 s[8:9], |v0|, s16
	v_lshlrev_b32_e32 v9, 20, v9
	v_or_b32_e32 v2, v2, v8
	v_cndmask_b32_e64 v8, 0, 1, s[8:9]
	v_cmp_gt_f32_e64 s[8:9], |v1|, s16
	v_or_b32_e32 v6, v6, v9
	v_cmp_gt_f32_e64 vcc, |v1|, s17
	v_cndmask_b32_e64 v9, 0, 1, s[8:9]
	v_cmp_gt_f32_e64 s[8:9], |v0|, 0.5
	s_nop 1
	v_cndmask_b32_e64 v10, 0, 1, s[8:9]
	v_cmp_gt_f32_e64 s[8:9], |v1|, 0.5
	s_nop 1
	v_cndmask_b32_e64 v11, 0, 1, s[8:9]
	v_addc_co_u32_e32 v9, vcc, v9, v11, vcc
	v_cmp_gt_f32_e64 vcc, |v0|, s17
	v_cmp_gt_f32_e64 s[8:9], |v1|, s19
	s_nop 0
	v_addc_co_u32_e32 v8, vcc, v8, v10, vcc
	v_cndmask_b32_e64 v10, 0, 1, s[8:9]
	v_cmp_gt_f32_e64 s[8:9], |v0|, s19
	v_cmp_gt_f32_e64 vcc, |v0|, s18
	s_nop 0
	v_cndmask_b32_e64 v11, 0, 1, s[8:9]
	v_addc_co_u32_e32 v8, vcc, v8, v11, vcc
	v_cmp_gt_f32_e64 vcc, |v1|, s18
	v_cmp_gt_f32_e64 s[8:9], |v0|, s20
	s_nop 0
	v_addc_co_u32_e32 v9, vcc, v9, v10, vcc
	v_cndmask_b32_e64 v10, 0, 1, s[8:9]
	v_cmp_gt_f32_e64 s[8:9], |v1|, s20
	v_cmp_gt_f32_e64 vcc, |v1|, s21
	v_lshrrev_b32_e32 v1, 28, v1
	v_cndmask_b32_e64 v11, 0, 1, s[8:9]
	v_addc_co_u32_e32 v9, vcc, v9, v11, vcc
	v_cmp_gt_f32_e64 vcc, |v0|, s21
	v_lshrrev_b32_e32 v0, 28, v0
	v_and_b32_e32 v0, 8, v0
	v_addc_co_u32_e32 v8, vcc, v8, v10, vcc
	v_and_b32_e32 v1, 8, v1
	v_or_b32_sdwa v0, v8, v0 dst_sel:BYTE_3 dst_unused:UNUSED_PAD src0_sel:DWORD src1_sel:DWORD
	v_or_b32_sdwa v1, v9, v1 dst_sel:BYTE_3 dst_unused:UNUSED_PAD src0_sel:DWORD src1_sel:DWORD
	v_or_b32_e32 v8, v2, v0
	v_mov_b32_e32 v2, v7
	v_or_b32_e32 v6, v6, v1
	v_pk_mul_f32 v[0:1], v[2:3], v[4:5] op_sel_hi:[1,0]
	s_nop 0
	v_cmp_gt_f32_e64 s[8:9], |v1|, s16
	v_cmp_gt_f32_e64 vcc, |v0|, s17
	s_nop 0
	v_cndmask_b32_e64 v2, 0, 1, s[8:9]
	v_cmp_gt_f32_e64 s[8:9], |v0|, s16
	s_nop 1
	v_cndmask_b32_e64 v3, 0, 1, s[8:9]
	v_cmp_gt_f32_e64 s[8:9], |v1|, 0.5
	s_nop 1
	v_cndmask_b32_e64 v4, 0, 1, s[8:9]
	v_cmp_gt_f32_e64 s[8:9], |v0|, 0.5
	s_nop 1
	v_cndmask_b32_e64 v7, 0, 1, s[8:9]
	v_addc_co_u32_e32 v3, vcc, v3, v7, vcc
	v_cmp_gt_f32_e64 vcc, |v1|, s17
	v_cmp_gt_f32_e64 s[8:9], |v0|, s19
	s_nop 0
	v_addc_co_u32_e32 v2, vcc, v2, v4, vcc
	v_cndmask_b32_e64 v4, 0, 1, s[8:9]
	v_cmp_gt_f32_e64 s[8:9], |v1|, s19
	v_cmp_gt_f32_e64 vcc, |v1|, s18
	s_nop 0
	v_cndmask_b32_e64 v7, 0, 1, s[8:9]
	v_addc_co_u32_e32 v2, vcc, v2, v7, vcc
	v_cmp_gt_f32_e64 vcc, |v0|, s18
	v_cmp_gt_f32_e64 s[8:9], |v1|, s20
	s_nop 0
	v_addc_co_u32_e32 v3, vcc, v3, v4, vcc
	v_cndmask_b32_e64 v4, 0, 1, s[8:9]
	v_cmp_gt_f32_e64 s[8:9], |v0|, s20
	v_cmp_gt_f32_e64 vcc, |v0|, s21
	v_and_b32_e32 v0, 0x80000000, v0
	v_cndmask_b32_e64 v7, 0, 1, s[8:9]
	v_addc_co_u32_e32 v3, vcc, v3, v7, vcc
	v_cmp_gt_f32_e64 vcc, |v1|, s21
	v_lshlrev_b32_e32 v3, 28, v3
	v_and_b32_e32 v1, 0x80000000, v1
	v_addc_co_u32_e32 v2, vcc, v2, v4, vcc
	v_lshlrev_b32_e32 v2, 28, v2
	v_or_b32_e32 v1, v2, v1
	v_or_b32_e32 v0, v3, v0
	v_or_b32_e32 v1, v6, v1
	v_or_b32_e32 v0, v8, v0
	global_store_dwordx2 v[20:21], v[0:1], off
	s_and_saveexec_b64 s[8:9], s[6:7]
	s_cbranch_execz .LBB0_58
	v_ashrrev_i32_e32 v19, 31, v18
	v_lshl_add_u64 v[0:1], v[18:19], 2, s[88:89]
	global_store_dword v[0:1], v5, off
	s_branch .LBB0_58
